# MoE K-loop: first K-iteration peeled with C=0 MFMAs, per-unit accumulator zeroing removed
# speedup vs baseline: 1.0137x; 1.0067x over previous
.LBB0_2060:
	s_and_b64 s[2:3], s[54:55], exec
	v_readlane_b32 s84, v252, 29
	s_cselect_b32 s3, s65, s66
	s_cselect_b32 s2, s11, s84
	s_add_u32 s29, s52, 0x100
	s_addc_u32 s31, s53, 0
	s_add_u32 s40, s34, 0x80
	v_mov_b32_e32 v155, v1
	v_mov_b32_e32 v161, v1
	s_addc_u32 s41, s35, 0
	v_lshl_add_u64 v[134:135], s[40:41], 0, v[160:161]
	v_lshl_add_u64 v[136:137], s[40:41], 0, v[154:155]
	s_mov_b32 s13, -2
	s_mov_b64 s[52:53], 0
	v_mov_b32_e32 v0, s50
	v_readlane_b32 s85, v252, 30
	v_readlane_b32 s86, v252, 31
	v_readlane_b32 s87, v252, 32
	s_cmpk_lg_i32 s52, 0x200
	s_cselect_b64 s[40:41], -1, 0
	v_cmp_gt_i32_e32 vcc, 0, v0
	s_or_b64 vcc, s[40:41], vcc
	s_nor_b64 s[40:41], s[6:7], vcc
	v_cndmask_b32_e32 v138, -1, v0, vcc
	s_and_saveexec_b64 s[50:51], s[40:41]
	s_cbranch_execz .Lpk_2063
	v_lshl_add_u64 v[138:139], v[0:1], 2, s[14:15]
	global_atomic_add v[138:139], v204, off
	v_mov_b32_e32 v138, -1
.Lpk_2063:
	s_or_b64 exec, exec, s[50:51]
	s_add_i32 s33, s52, 0x180
	s_cmpk_eq_i32 s52, 0x700
	s_cselect_b64 s[40:41], -1, 0
	s_and_b64 s[40:41], s[40:41], exec
	s_cselect_b32 s56, 0x80, s33
	s_add_u32 s50, s52, 0x100
	s_addc_u32 s51, s53, 0
	s_cmpk_eq_i32 s52, 0x700
	s_cselect_b64 s[40:41], -1, 0
	s_and_b64 s[40:41], s[40:41], exec
	s_cselect_b32 s40, 0, s50
	s_add_u32 s33, s29, s52
	s_addc_u32 s41, s31, s53
	s_cmpk_eq_i32 s52, 0x700
	s_cselect_b64 vcc, -1, 0
	s_and_b64 s[46:47], vcc, exec
	s_cselect_b32 s54, s38, s33
	s_cselect_b32 s55, s39, s41
	s_add_i32 s33, 0, 0x10000
	v_add_u32_e32 v0, s33, v159
	s_add_i32 s41, 0, 0x14000
	ds_read_b128 v[140:143], v0
	ds_read_b128 v[144:147], v0 offset:1024
	ds_read_b128 v[162:165], v0 offset:2048
	ds_read_b128 v[166:169], v0 offset:3072
	v_add_u32_e32 v0, s41, v159
	ds_read_b128 v[170:173], v0
	ds_read_b128 v[190:193], v0 offset:1024
	ds_read_b128 v[194:197], v0 offset:2048
	ds_read_b128 v[198:201], v0 offset:3072
	v_lshl_add_u64 v[148:149], v[136:137], 0, s[52:53]
	s_add_i32 m0, s68, 0xc000
	ds_read_b128 v[224:227], v180
	ds_read_b128 v[228:231], v180 offset:1024
	ds_read_b128 v[232:235], v180 offset:2048
	ds_read_b128 v[236:239], v180 offset:3072
	ds_read_b128 v[240:243], v180 offset:4096
	ds_read_b128 v[244:247], v180 offset:5120
	ds_read_b128 v[182:185], v180 offset:6144
	ds_read_b128 v[218:221], v180 offset:7168
	global_load_lds_dwordx4 v[148:149], off
	v_lshl_add_u64 v[148:149], v[134:135], 0, s[52:53]
	s_add_i32 m0, s68, 0xe000
	s_nop 0
	global_load_lds_dwordx4 v[148:149], off
	s_cmp_lg_u32 s32, 0
	s_cbranch_scc1 .Lpk_mwd_0
	s_waitcnt vmcnt(8)
.Lpk_mwd_0:
	s_waitcnt lgkmcnt(0)
	s_barrier
	s_setprio 1
	s_waitcnt lgkmcnt(0)
	v_mfma_f32_16x16x32_bf16 v[130:133], v[140:143], v[224:227], 0
	v_mfma_f32_16x16x32_bf16 v[126:129], v[162:165], v[224:227], 0
	v_mfma_f32_16x16x32_bf16 v[122:125], v[140:143], v[232:235], 0
	v_mfma_f32_16x16x32_bf16 v[118:121], v[162:165], v[232:235], 0
	v_mfma_f32_16x16x32_bf16 v[114:117], v[140:143], v[240:243], 0
	v_mfma_f32_16x16x32_bf16 v[110:113], v[162:165], v[240:243], 0
	v_mfma_f32_16x16x32_bf16 v[106:109], v[140:143], v[182:185], 0
	v_mfma_f32_16x16x32_bf16 v[102:105], v[162:165], v[182:185], 0
	v_mfma_f32_16x16x32_bf16 v[130:133], v[144:147], v[228:231], v[130:133]
	v_mfma_f32_16x16x32_bf16 v[126:129], v[166:169], v[228:231], v[126:129]
	v_mfma_f32_16x16x32_bf16 v[122:125], v[144:147], v[236:239], v[122:125]
	v_mfma_f32_16x16x32_bf16 v[118:121], v[166:169], v[236:239], v[118:121]
	v_mfma_f32_16x16x32_bf16 v[114:117], v[144:147], v[244:247], v[114:117]
	v_mfma_f32_16x16x32_bf16 v[110:113], v[166:169], v[244:247], v[110:113]
	v_mfma_f32_16x16x32_bf16 v[106:109], v[144:147], v[218:221], v[106:109]
	v_mfma_f32_16x16x32_bf16 v[102:105], v[166:169], v[218:221], v[102:105]
	s_setprio 0
	s_setprio 1
	v_mfma_f32_16x16x32_bf16 v[98:101], v[170:173], v[224:227], 0
	v_mfma_f32_16x16x32_bf16 v[94:97], v[194:197], v[224:227], 0
	v_mfma_f32_16x16x32_bf16 v[90:93], v[170:173], v[232:235], 0
	v_mfma_f32_16x16x32_bf16 v[86:89], v[194:197], v[232:235], 0
	v_mfma_f32_16x16x32_bf16 v[82:85], v[170:173], v[240:243], 0
	v_mfma_f32_16x16x32_bf16 v[78:81], v[194:197], v[240:243], 0
	v_mfma_f32_16x16x32_bf16 v[74:77], v[170:173], v[182:185], 0
	v_mfma_f32_16x16x32_bf16 v[70:73], v[194:197], v[182:185], 0
	v_mfma_f32_16x16x32_bf16 v[98:101], v[190:193], v[228:231], v[98:101]
	v_mfma_f32_16x16x32_bf16 v[94:97], v[198:201], v[228:231], v[94:97]
	v_mfma_f32_16x16x32_bf16 v[90:93], v[190:193], v[236:239], v[90:93]
	v_mfma_f32_16x16x32_bf16 v[86:89], v[198:201], v[236:239], v[86:89]
	v_mfma_f32_16x16x32_bf16 v[82:85], v[190:193], v[244:247], v[82:85]
	v_mfma_f32_16x16x32_bf16 v[78:81], v[198:201], v[244:247], v[78:81]
	v_mfma_f32_16x16x32_bf16 v[74:77], v[190:193], v[218:221], v[74:77]
	v_mfma_f32_16x16x32_bf16 v[70:73], v[198:201], v[218:221], v[70:73]
	s_setprio 0
	s_barrier
	s_add_i32 s33, s33, s67
	v_lshl_add_u64 v[148:149], s[54:55], 0, v[150:151]
	s_mov_b32 m0, s33
	ds_read_b128 v[182:185], v180 offset:16384
	ds_read_b128 v[218:221], v180 offset:17408
	ds_read_b128 v[224:227], v180 offset:18432
	ds_read_b128 v[228:231], v180 offset:19456
	ds_read_b128 v[232:235], v180 offset:20480
	ds_read_b128 v[236:239], v180 offset:21504
	ds_read_b128 v[240:243], v180 offset:22528
	ds_read_b128 v[244:247], v180 offset:23552
	global_load_lds_dwordx4 v[148:149], off
	s_add_i32 m0, s33, 0x2000
	s_add_u32 s46, s54, 0x40000
	v_lshl_add_u64 v[202:203], s[54:55], 0, v[152:153]
	s_addc_u32 s47, s55, 0
	s_add_i32 s33, s41, s67
	global_load_lds_dwordx4 v[202:203], off
	v_lshl_add_u64 v[210:211], s[46:47], 0, v[150:151]
	s_mov_b32 m0, s33
	v_cndmask_b32_e32 v0, v158, v188, vcc
	global_load_lds_dwordx4 v[210:211], off
	v_lshl_add_u64 v[210:211], s[46:47], 0, v[152:153]
	s_add_i32 m0, s33, 0x2000
	s_and_b64 s[46:47], s[42:43], vcc
	s_and_b64 s[46:47], s[46:47], exec
	s_cselect_b32 s44, s2, s34
	s_cselect_b32 s33, s3, s35
	s_add_u32 s40, s44, s40
	global_load_lds_dwordx4 v[210:211], off
	s_addc_u32 s41, s33, 0
	s_mov_b32 m0, s68
	v_cndmask_b32_e32 v139, v156, v186, vcc
	global_load_lds_dwordx4 v0, s[40:41]
	s_mov_b32 m0, s69
	s_nop 0
	global_load_lds_dwordx4 v139, s[40:41]
	s_cmp_lg_u32 s32, 0
	s_cbranch_scc1 .Lpk_mwd_1
	s_waitcnt vmcnt(8)
.Lpk_mwd_1:
	s_waitcnt lgkmcnt(0)
	s_barrier
	s_setprio 1
	s_waitcnt lgkmcnt(0)
	v_mfma_f32_16x16x32_bf16 v[66:69], v[140:143], v[182:185], 0
	v_mfma_f32_16x16x32_bf16 v[62:65], v[162:165], v[182:185], 0
	v_mfma_f32_16x16x32_bf16 v[58:61], v[140:143], v[224:227], 0
	v_mfma_f32_16x16x32_bf16 v[54:57], v[162:165], v[224:227], 0
	v_mfma_f32_16x16x32_bf16 v[50:53], v[140:143], v[232:235], 0
	v_mfma_f32_16x16x32_bf16 v[46:49], v[162:165], v[232:235], 0
	v_mfma_f32_16x16x32_bf16 v[42:45], v[140:143], v[240:243], 0
	v_mfma_f32_16x16x32_bf16 v[38:41], v[162:165], v[240:243], 0
	v_mfma_f32_16x16x32_bf16 v[66:69], v[144:147], v[218:221], v[66:69]
	v_mfma_f32_16x16x32_bf16 v[62:65], v[166:169], v[218:221], v[62:65]
	v_mfma_f32_16x16x32_bf16 v[58:61], v[144:147], v[228:231], v[58:61]
	v_mfma_f32_16x16x32_bf16 v[54:57], v[166:169], v[228:231], v[54:57]
	v_mfma_f32_16x16x32_bf16 v[50:53], v[144:147], v[236:239], v[50:53]
	v_mfma_f32_16x16x32_bf16 v[46:49], v[166:169], v[236:239], v[46:49]
	v_mfma_f32_16x16x32_bf16 v[42:45], v[144:147], v[244:247], v[42:45]
	v_mfma_f32_16x16x32_bf16 v[38:41], v[166:169], v[244:247], v[38:41]
	s_setprio 0
	s_setprio 1
	v_mfma_f32_16x16x32_bf16 v[30:33], v[170:173], v[182:185], 0
	v_mfma_f32_16x16x32_bf16 v[26:29], v[194:197], v[182:185], 0
	v_mfma_f32_16x16x32_bf16 v[22:25], v[170:173], v[224:227], 0
	v_mfma_f32_16x16x32_bf16 v[18:21], v[194:197], v[224:227], 0
	v_mfma_f32_16x16x32_bf16 v[14:17], v[170:173], v[232:235], 0
	v_mfma_f32_16x16x32_bf16 v[10:13], v[194:197], v[232:235], 0
	v_mfma_f32_16x16x32_bf16 v[6:9], v[170:173], v[240:243], 0
	v_mfma_f32_16x16x32_bf16 v[2:5], v[194:197], v[240:243], 0
	v_mfma_f32_16x16x32_bf16 v[30:33], v[190:193], v[218:221], v[30:33]
	v_mfma_f32_16x16x32_bf16 v[26:29], v[198:201], v[218:221], v[26:29]
	v_mfma_f32_16x16x32_bf16 v[22:25], v[190:193], v[228:231], v[22:25]
	v_mfma_f32_16x16x32_bf16 v[18:21], v[198:201], v[228:231], v[18:21]
	v_mfma_f32_16x16x32_bf16 v[14:17], v[190:193], v[236:239], v[14:17]
	v_mfma_f32_16x16x32_bf16 v[10:13], v[198:201], v[236:239], v[10:13]
	v_mfma_f32_16x16x32_bf16 v[6:9], v[190:193], v[244:247], v[6:9]
	v_mfma_f32_16x16x32_bf16 v[2:5], v[198:201], v[244:247], v[2:5]
	s_setprio 0
	s_barrier
	s_add_i32 s46, 0, 0x18000
	v_add_u32_e32 v155, s46, v159
	s_add_i32 s47, 0, 0x1c000
	ds_read_b128 v[140:143], v155
	ds_read_b128 v[144:147], v155 offset:1024
	ds_read_b128 v[162:165], v155 offset:2048
	ds_read_b128 v[166:169], v155 offset:3072
	v_add_u32_e32 v155, s47, v159
	ds_read_b128 v[170:173], v155
	ds_read_b128 v[182:185], v155 offset:1024
	ds_read_b128 v[190:193], v155 offset:2048
	ds_read_b128 v[194:197], v155 offset:3072
	s_mov_b32 m0, s70
	v_cndmask_b32_e32 v155, v154, v181, vcc
	ds_read_b128 v[198:201], v180 offset:32768
	ds_read_b128 v[218:221], v180 offset:33792
	ds_read_b128 v[224:227], v180 offset:34816
	ds_read_b128 v[228:231], v180 offset:35840
	ds_read_b128 v[232:235], v180 offset:36864
	ds_read_b128 v[236:239], v180 offset:37888
	ds_read_b128 v[240:243], v180 offset:38912
	ds_read_b128 v[244:247], v180 offset:39936
	global_load_lds_dwordx4 v155, s[40:41]
	v_cndmask_b32_e32 v155, v160, v187, vcc
	s_mov_b32 m0, s71
	s_nop 0
	global_load_lds_dwordx4 v155, s[40:41]
	s_waitcnt vmcnt(8)
	s_waitcnt lgkmcnt(0)
	s_barrier
	s_setprio 1
	s_waitcnt lgkmcnt(0)
	v_mfma_f32_16x16x32_bf16 v[130:133], v[140:143], v[198:201], v[130:133]
	v_mfma_f32_16x16x32_bf16 v[126:129], v[162:165], v[198:201], v[126:129]
	v_mfma_f32_16x16x32_bf16 v[122:125], v[140:143], v[224:227], v[122:125]
	v_mfma_f32_16x16x32_bf16 v[118:121], v[162:165], v[224:227], v[118:121]
	v_mfma_f32_16x16x32_bf16 v[114:117], v[140:143], v[232:235], v[114:117]
	v_mfma_f32_16x16x32_bf16 v[110:113], v[162:165], v[232:235], v[110:113]
	v_mfma_f32_16x16x32_bf16 v[106:109], v[140:143], v[240:243], v[106:109]
	v_mfma_f32_16x16x32_bf16 v[102:105], v[162:165], v[240:243], v[102:105]
	v_mfma_f32_16x16x32_bf16 v[130:133], v[144:147], v[218:221], v[130:133]
	v_mfma_f32_16x16x32_bf16 v[126:129], v[166:169], v[218:221], v[126:129]
	v_mfma_f32_16x16x32_bf16 v[122:125], v[144:147], v[228:231], v[122:125]
	v_mfma_f32_16x16x32_bf16 v[118:121], v[166:169], v[228:231], v[118:121]
	v_mfma_f32_16x16x32_bf16 v[114:117], v[144:147], v[236:239], v[114:117]
	v_mfma_f32_16x16x32_bf16 v[110:113], v[166:169], v[236:239], v[110:113]
	v_mfma_f32_16x16x32_bf16 v[106:109], v[144:147], v[244:247], v[106:109]
	v_mfma_f32_16x16x32_bf16 v[102:105], v[166:169], v[244:247], v[102:105]
	s_setprio 0
	s_setprio 1
	v_mfma_f32_16x16x32_bf16 v[98:101], v[170:173], v[198:201], v[98:101]
	v_mfma_f32_16x16x32_bf16 v[94:97], v[190:193], v[198:201], v[94:97]
	v_mfma_f32_16x16x32_bf16 v[90:93], v[170:173], v[224:227], v[90:93]
	v_mfma_f32_16x16x32_bf16 v[86:89], v[190:193], v[224:227], v[86:89]
	v_mfma_f32_16x16x32_bf16 v[82:85], v[170:173], v[232:235], v[82:85]
	v_mfma_f32_16x16x32_bf16 v[78:81], v[190:193], v[232:235], v[78:81]
	v_mfma_f32_16x16x32_bf16 v[74:77], v[170:173], v[240:243], v[74:77]
	v_mfma_f32_16x16x32_bf16 v[70:73], v[190:193], v[240:243], v[70:73]
	v_mfma_f32_16x16x32_bf16 v[98:101], v[182:185], v[218:221], v[98:101]
	v_mfma_f32_16x16x32_bf16 v[94:97], v[194:197], v[218:221], v[94:97]
	v_mfma_f32_16x16x32_bf16 v[90:93], v[182:185], v[228:231], v[90:93]
	v_mfma_f32_16x16x32_bf16 v[86:89], v[194:197], v[228:231], v[86:89]
	v_mfma_f32_16x16x32_bf16 v[82:85], v[182:185], v[236:239], v[82:85]
	v_mfma_f32_16x16x32_bf16 v[78:81], v[194:197], v[236:239], v[78:81]
	v_mfma_f32_16x16x32_bf16 v[74:77], v[182:185], v[244:247], v[74:77]
	v_mfma_f32_16x16x32_bf16 v[70:73], v[194:197], v[244:247], v[70:73]
	s_setprio 0
	s_barrier
	s_mov_b64 s[52:53], 0x80
	s_add_i32 s40, s46, s67
	v_lshl_add_u64 v[148:149], v[148:149], 0, s[52:53]
	s_mov_b32 m0, s40
	ds_read_b128 v[198:201], v180 offset:49152
	ds_read_b128 v[218:221], v180 offset:50176
	ds_read_b128 v[224:227], v180 offset:51200
	ds_read_b128 v[228:231], v180 offset:52224
	ds_read_b128 v[232:235], v180 offset:53248
	ds_read_b128 v[236:239], v180 offset:54272
	ds_read_b128 v[240:243], v180 offset:55296
	ds_read_b128 v[244:247], v180 offset:56320
	global_load_lds_dwordx4 v[148:149], off
	s_add_i32 m0, s40, 0x2000
	s_add_u32 s40, s54, 0x40080
	v_lshl_add_u64 v[148:149], v[202:203], 0, s[52:53]
	s_addc_u32 s41, s55, 0
	s_add_i32 s46, s47, s67
	global_load_lds_dwordx4 v[148:149], off
	v_lshl_add_u64 v[148:149], s[40:41], 0, v[150:151]
	s_mov_b32 m0, s46
	s_nop 0
	global_load_lds_dwordx4 v[148:149], off
	s_add_i32 m0, s46, 0x2000
	v_lshl_add_u64 v[148:149], s[40:41], 0, v[152:153]
	s_add_u32 s40, s44, s56
	global_load_lds_dwordx4 v[148:149], off
	s_addc_u32 s41, s33, 0
	s_mov_b32 m0, s76
	s_nop 0
	global_load_lds_dwordx4 v0, s[40:41]
	s_mov_b32 m0, s77
	s_nop 0
	global_load_lds_dwordx4 v139, s[40:41]
	s_waitcnt vmcnt(8)
	v_lshl_add_u32 v181, v250, 11, v176
	v_lshl_add_u32 v186, v249, 11, v177
	v_lshl_add_u32 v188, v248, 11, v176
	v_lshl_add_u32 v187, v223, 11, v177
	s_waitcnt lgkmcnt(0)
	s_barrier
	s_setprio 1
	s_waitcnt lgkmcnt(0)
	v_mfma_f32_16x16x32_bf16 v[66:69], v[140:143], v[198:201], v[66:69]
	v_mfma_f32_16x16x32_bf16 v[62:65], v[162:165], v[198:201], v[62:65]
	v_mfma_f32_16x16x32_bf16 v[58:61], v[140:143], v[224:227], v[58:61]
	v_mfma_f32_16x16x32_bf16 v[54:57], v[162:165], v[224:227], v[54:57]
	v_mfma_f32_16x16x32_bf16 v[50:53], v[140:143], v[232:235], v[50:53]
	v_mfma_f32_16x16x32_bf16 v[46:49], v[162:165], v[232:235], v[46:49]
	v_mfma_f32_16x16x32_bf16 v[42:45], v[140:143], v[240:243], v[42:45]
	v_mfma_f32_16x16x32_bf16 v[38:41], v[162:165], v[240:243], v[38:41]
	v_mfma_f32_16x16x32_bf16 v[66:69], v[144:147], v[218:221], v[66:69]
	v_mfma_f32_16x16x32_bf16 v[62:65], v[166:169], v[218:221], v[62:65]
	v_mfma_f32_16x16x32_bf16 v[58:61], v[144:147], v[228:231], v[58:61]
	v_mfma_f32_16x16x32_bf16 v[54:57], v[166:169], v[228:231], v[54:57]
	v_mfma_f32_16x16x32_bf16 v[50:53], v[144:147], v[236:239], v[50:53]
	v_mfma_f32_16x16x32_bf16 v[46:49], v[166:169], v[236:239], v[46:49]
	v_mfma_f32_16x16x32_bf16 v[42:45], v[144:147], v[244:247], v[42:45]
	v_mfma_f32_16x16x32_bf16 v[38:41], v[166:169], v[244:247], v[38:41]
	s_setprio 0
	s_setprio 1
	v_mfma_f32_16x16x32_bf16 v[30:33], v[170:173], v[198:201], v[30:33]
	v_mfma_f32_16x16x32_bf16 v[26:29], v[190:193], v[198:201], v[26:29]
	v_mfma_f32_16x16x32_bf16 v[22:25], v[170:173], v[224:227], v[22:25]
	v_mfma_f32_16x16x32_bf16 v[18:21], v[190:193], v[224:227], v[18:21]
	v_mfma_f32_16x16x32_bf16 v[14:17], v[170:173], v[232:235], v[14:17]
	v_mfma_f32_16x16x32_bf16 v[10:13], v[190:193], v[232:235], v[10:13]
	v_mfma_f32_16x16x32_bf16 v[6:9], v[170:173], v[240:243], v[6:9]
	v_mfma_f32_16x16x32_bf16 v[2:5], v[190:193], v[240:243], v[2:5]
	v_mfma_f32_16x16x32_bf16 v[30:33], v[182:185], v[218:221], v[30:33]
	v_mfma_f32_16x16x32_bf16 v[26:29], v[194:197], v[218:221], v[26:29]
	v_mfma_f32_16x16x32_bf16 v[22:25], v[182:185], v[228:231], v[22:25]
	v_mfma_f32_16x16x32_bf16 v[18:21], v[194:197], v[228:231], v[18:21]
	v_mfma_f32_16x16x32_bf16 v[14:17], v[182:185], v[236:239], v[14:17]
	v_mfma_f32_16x16x32_bf16 v[10:13], v[194:197], v[236:239], v[10:13]
	v_mfma_f32_16x16x32_bf16 v[6:9], v[182:185], v[244:247], v[6:9]
	v_mfma_f32_16x16x32_bf16 v[2:5], v[194:197], v[244:247], v[2:5]
	s_setprio 0
	s_barrier
	s_add_i32 s13, s13, 2
	s_mov_b64 s[52:53], s[50:51]
	v_mov_b32_e32 v0, v138

.LBB0_2063:
	s_or_b64 exec, exec, s[50:51]
	s_add_i32 s33, s52, 0x180
	s_cmpk_eq_i32 s52, 0x700
	s_cselect_b64 s[40:41], -1, 0
	s_and_b64 s[40:41], s[40:41], exec
	s_cselect_b32 s56, 0x80, s33
	s_add_u32 s50, s52, 0x100
	s_addc_u32 s51, s53, 0
	s_cmpk_eq_i32 s52, 0x700
	s_cselect_b64 s[40:41], -1, 0
	s_and_b64 s[40:41], s[40:41], exec
	s_cselect_b32 s40, 0, s50
	s_add_u32 s33, s29, s52
	s_addc_u32 s41, s31, s53
	s_cmpk_eq_i32 s52, 0x700
	s_cselect_b64 vcc, -1, 0
	s_and_b64 s[46:47], vcc, exec
	s_cselect_b32 s54, s38, s33
	s_cselect_b32 s55, s39, s41
	s_add_i32 s33, 0, 0x10000
	v_add_u32_e32 v0, s33, v159
	s_add_i32 s41, 0, 0x14000
	ds_read_b128 v[140:143], v0
	ds_read_b128 v[144:147], v0 offset:1024
	ds_read_b128 v[162:165], v0 offset:2048
	ds_read_b128 v[166:169], v0 offset:3072
	v_add_u32_e32 v0, s41, v159
	ds_read_b128 v[170:173], v0
	ds_read_b128 v[190:193], v0 offset:1024
	ds_read_b128 v[194:197], v0 offset:2048
	ds_read_b128 v[198:201], v0 offset:3072
	v_lshl_add_u64 v[148:149], v[136:137], 0, s[52:53]
	s_add_i32 m0, s68, 0xc000
	ds_read_b128 v[224:227], v180
	ds_read_b128 v[228:231], v180 offset:1024
	ds_read_b128 v[232:235], v180 offset:2048
	ds_read_b128 v[236:239], v180 offset:3072
	ds_read_b128 v[240:243], v180 offset:4096
	ds_read_b128 v[244:247], v180 offset:5120
	ds_read_b128 v[182:185], v180 offset:6144
	ds_read_b128 v[218:221], v180 offset:7168
	global_load_lds_dwordx4 v[148:149], off
	v_lshl_add_u64 v[148:149], v[134:135], 0, s[52:53]
	s_add_i32 m0, s68, 0xe000
	s_nop 0
	global_load_lds_dwordx4 v[148:149], off
	s_waitcnt vmcnt(8)
	s_waitcnt lgkmcnt(0)
	s_barrier
	s_setprio 1
	s_waitcnt lgkmcnt(0)
	v_mfma_f32_16x16x32_bf16 v[130:133], v[140:143], v[224:227], v[130:133]
	v_mfma_f32_16x16x32_bf16 v[126:129], v[162:165], v[224:227], v[126:129]
	v_mfma_f32_16x16x32_bf16 v[122:125], v[140:143], v[232:235], v[122:125]
	v_mfma_f32_16x16x32_bf16 v[118:121], v[162:165], v[232:235], v[118:121]
	v_mfma_f32_16x16x32_bf16 v[114:117], v[140:143], v[240:243], v[114:117]
	v_mfma_f32_16x16x32_bf16 v[110:113], v[162:165], v[240:243], v[110:113]
	v_mfma_f32_16x16x32_bf16 v[106:109], v[140:143], v[182:185], v[106:109]
	v_mfma_f32_16x16x32_bf16 v[102:105], v[162:165], v[182:185], v[102:105]
	v_mfma_f32_16x16x32_bf16 v[130:133], v[144:147], v[228:231], v[130:133]
	v_mfma_f32_16x16x32_bf16 v[126:129], v[166:169], v[228:231], v[126:129]
	v_mfma_f32_16x16x32_bf16 v[122:125], v[144:147], v[236:239], v[122:125]
	v_mfma_f32_16x16x32_bf16 v[118:121], v[166:169], v[236:239], v[118:121]
	v_mfma_f32_16x16x32_bf16 v[114:117], v[144:147], v[244:247], v[114:117]
	v_mfma_f32_16x16x32_bf16 v[110:113], v[166:169], v[244:247], v[110:113]
	v_mfma_f32_16x16x32_bf16 v[106:109], v[144:147], v[218:221], v[106:109]
	v_mfma_f32_16x16x32_bf16 v[102:105], v[166:169], v[218:221], v[102:105]
	s_setprio 0
	s_setprio 1
	v_mfma_f32_16x16x32_bf16 v[98:101], v[170:173], v[224:227], v[98:101]
	v_mfma_f32_16x16x32_bf16 v[94:97], v[194:197], v[224:227], v[94:97]
	v_mfma_f32_16x16x32_bf16 v[90:93], v[170:173], v[232:235], v[90:93]
	v_mfma_f32_16x16x32_bf16 v[86:89], v[194:197], v[232:235], v[86:89]
	v_mfma_f32_16x16x32_bf16 v[82:85], v[170:173], v[240:243], v[82:85]
	v_mfma_f32_16x16x32_bf16 v[78:81], v[194:197], v[240:243], v[78:81]
	v_mfma_f32_16x16x32_bf16 v[74:77], v[170:173], v[182:185], v[74:77]
	v_mfma_f32_16x16x32_bf16 v[70:73], v[194:197], v[182:185], v[70:73]
	v_mfma_f32_16x16x32_bf16 v[98:101], v[190:193], v[228:231], v[98:101]
	v_mfma_f32_16x16x32_bf16 v[94:97], v[198:201], v[228:231], v[94:97]
	v_mfma_f32_16x16x32_bf16 v[90:93], v[190:193], v[236:239], v[90:93]
	v_mfma_f32_16x16x32_bf16 v[86:89], v[198:201], v[236:239], v[86:89]
	v_mfma_f32_16x16x32_bf16 v[82:85], v[190:193], v[244:247], v[82:85]
	v_mfma_f32_16x16x32_bf16 v[78:81], v[198:201], v[244:247], v[78:81]
	v_mfma_f32_16x16x32_bf16 v[74:77], v[190:193], v[218:221], v[74:77]
	v_mfma_f32_16x16x32_bf16 v[70:73], v[198:201], v[218:221], v[70:73]
	s_setprio 0
	s_barrier
	s_add_i32 s33, s33, s67
	v_lshl_add_u64 v[148:149], s[54:55], 0, v[150:151]
	s_mov_b32 m0, s33
	ds_read_b128 v[182:185], v180 offset:16384
	ds_read_b128 v[218:221], v180 offset:17408
	ds_read_b128 v[224:227], v180 offset:18432
	ds_read_b128 v[228:231], v180 offset:19456
	ds_read_b128 v[232:235], v180 offset:20480
	ds_read_b128 v[236:239], v180 offset:21504
	ds_read_b128 v[240:243], v180 offset:22528
	ds_read_b128 v[244:247], v180 offset:23552
	global_load_lds_dwordx4 v[148:149], off
	s_add_i32 m0, s33, 0x2000
	s_add_u32 s46, s54, 0x40000
	v_lshl_add_u64 v[202:203], s[54:55], 0, v[152:153]
	s_addc_u32 s47, s55, 0
	s_add_i32 s33, s41, s67
	global_load_lds_dwordx4 v[202:203], off
	v_lshl_add_u64 v[210:211], s[46:47], 0, v[150:151]
	s_mov_b32 m0, s33
	v_cndmask_b32_e32 v0, v158, v188, vcc
	global_load_lds_dwordx4 v[210:211], off
	v_lshl_add_u64 v[210:211], s[46:47], 0, v[152:153]
	s_add_i32 m0, s33, 0x2000
	s_and_b64 s[46:47], s[42:43], vcc
	s_and_b64 s[46:47], s[46:47], exec
	s_cselect_b32 s44, s2, s34
	s_cselect_b32 s33, s3, s35
	s_add_u32 s40, s44, s40
	global_load_lds_dwordx4 v[210:211], off
	s_addc_u32 s41, s33, 0
	s_mov_b32 m0, s68
	v_cndmask_b32_e32 v139, v156, v186, vcc
	global_load_lds_dwordx4 v0, s[40:41]
	s_mov_b32 m0, s69
	s_nop 0
	global_load_lds_dwordx4 v139, s[40:41]
	s_waitcnt vmcnt(8)
	s_waitcnt lgkmcnt(0)
	s_barrier
	s_setprio 1
	s_waitcnt lgkmcnt(0)
	v_mfma_f32_16x16x32_bf16 v[66:69], v[140:143], v[182:185], v[66:69]
	v_mfma_f32_16x16x32_bf16 v[62:65], v[162:165], v[182:185], v[62:65]
	v_mfma_f32_16x16x32_bf16 v[58:61], v[140:143], v[224:227], v[58:61]
	v_mfma_f32_16x16x32_bf16 v[54:57], v[162:165], v[224:227], v[54:57]
	v_mfma_f32_16x16x32_bf16 v[50:53], v[140:143], v[232:235], v[50:53]
	v_mfma_f32_16x16x32_bf16 v[46:49], v[162:165], v[232:235], v[46:49]
	v_mfma_f32_16x16x32_bf16 v[42:45], v[140:143], v[240:243], v[42:45]
	v_mfma_f32_16x16x32_bf16 v[38:41], v[162:165], v[240:243], v[38:41]
	v_mfma_f32_16x16x32_bf16 v[66:69], v[144:147], v[218:221], v[66:69]
	v_mfma_f32_16x16x32_bf16 v[62:65], v[166:169], v[218:221], v[62:65]
	v_mfma_f32_16x16x32_bf16 v[58:61], v[144:147], v[228:231], v[58:61]
	v_mfma_f32_16x16x32_bf16 v[54:57], v[166:169], v[228:231], v[54:57]
	v_mfma_f32_16x16x32_bf16 v[50:53], v[144:147], v[236:239], v[50:53]
	v_mfma_f32_16x16x32_bf16 v[46:49], v[166:169], v[236:239], v[46:49]
	v_mfma_f32_16x16x32_bf16 v[42:45], v[144:147], v[244:247], v[42:45]
	v_mfma_f32_16x16x32_bf16 v[38:41], v[166:169], v[244:247], v[38:41]
	s_setprio 0
	s_setprio 1
	v_mfma_f32_16x16x32_bf16 v[30:33], v[170:173], v[182:185], v[30:33]
	v_mfma_f32_16x16x32_bf16 v[26:29], v[194:197], v[182:185], v[26:29]
	v_mfma_f32_16x16x32_bf16 v[22:25], v[170:173], v[224:227], v[22:25]
	v_mfma_f32_16x16x32_bf16 v[18:21], v[194:197], v[224:227], v[18:21]
	v_mfma_f32_16x16x32_bf16 v[14:17], v[170:173], v[232:235], v[14:17]
	v_mfma_f32_16x16x32_bf16 v[10:13], v[194:197], v[232:235], v[10:13]
	v_mfma_f32_16x16x32_bf16 v[6:9], v[170:173], v[240:243], v[6:9]
	v_mfma_f32_16x16x32_bf16 v[2:5], v[194:197], v[240:243], v[2:5]
	v_mfma_f32_16x16x32_bf16 v[30:33], v[190:193], v[218:221], v[30:33]
	v_mfma_f32_16x16x32_bf16 v[26:29], v[198:201], v[218:221], v[26:29]
	v_mfma_f32_16x16x32_bf16 v[22:25], v[190:193], v[228:231], v[22:25]
	v_mfma_f32_16x16x32_bf16 v[18:21], v[198:201], v[228:231], v[18:21]
	v_mfma_f32_16x16x32_bf16 v[14:17], v[190:193], v[236:239], v[14:17]
	v_mfma_f32_16x16x32_bf16 v[10:13], v[198:201], v[236:239], v[10:13]
	v_mfma_f32_16x16x32_bf16 v[6:9], v[190:193], v[244:247], v[6:9]
	v_mfma_f32_16x16x32_bf16 v[2:5], v[198:201], v[244:247], v[2:5]
	s_setprio 0
	s_barrier
	s_add_i32 s46, 0, 0x18000
	v_add_u32_e32 v155, s46, v159
	s_add_i32 s47, 0, 0x1c000
	ds_read_b128 v[140:143], v155
	ds_read_b128 v[144:147], v155 offset:1024
	ds_read_b128 v[162:165], v155 offset:2048
	ds_read_b128 v[166:169], v155 offset:3072
	v_add_u32_e32 v155, s47, v159
	ds_read_b128 v[170:173], v155
	ds_read_b128 v[182:185], v155 offset:1024
	ds_read_b128 v[190:193], v155 offset:2048
	ds_read_b128 v[194:197], v155 offset:3072
	s_mov_b32 m0, s70
	v_cndmask_b32_e32 v155, v154, v181, vcc
	ds_read_b128 v[198:201], v180 offset:32768
	ds_read_b128 v[218:221], v180 offset:33792
	ds_read_b128 v[224:227], v180 offset:34816
	ds_read_b128 v[228:231], v180 offset:35840
	ds_read_b128 v[232:235], v180 offset:36864
	ds_read_b128 v[236:239], v180 offset:37888
	ds_read_b128 v[240:243], v180 offset:38912
	ds_read_b128 v[244:247], v180 offset:39936
	global_load_lds_dwordx4 v155, s[40:41]
	v_cndmask_b32_e32 v155, v160, v187, vcc
	s_mov_b32 m0, s71
	s_nop 0
	global_load_lds_dwordx4 v155, s[40:41]
	s_waitcnt vmcnt(8)
	s_waitcnt lgkmcnt(0)
	s_barrier
	s_setprio 1
	s_waitcnt lgkmcnt(0)
	v_mfma_f32_16x16x32_bf16 v[130:133], v[140:143], v[198:201], v[130:133]
	v_mfma_f32_16x16x32_bf16 v[126:129], v[162:165], v[198:201], v[126:129]
	v_mfma_f32_16x16x32_bf16 v[122:125], v[140:143], v[224:227], v[122:125]
	v_mfma_f32_16x16x32_bf16 v[118:121], v[162:165], v[224:227], v[118:121]
	v_mfma_f32_16x16x32_bf16 v[114:117], v[140:143], v[232:235], v[114:117]
	v_mfma_f32_16x16x32_bf16 v[110:113], v[162:165], v[232:235], v[110:113]
	v_mfma_f32_16x16x32_bf16 v[106:109], v[140:143], v[240:243], v[106:109]
	v_mfma_f32_16x16x32_bf16 v[102:105], v[162:165], v[240:243], v[102:105]
	v_mfma_f32_16x16x32_bf16 v[130:133], v[144:147], v[218:221], v[130:133]
	v_mfma_f32_16x16x32_bf16 v[126:129], v[166:169], v[218:221], v[126:129]
	v_mfma_f32_16x16x32_bf16 v[122:125], v[144:147], v[228:231], v[122:125]
	v_mfma_f32_16x16x32_bf16 v[118:121], v[166:169], v[228:231], v[118:121]
	v_mfma_f32_16x16x32_bf16 v[114:117], v[144:147], v[236:239], v[114:117]
	v_mfma_f32_16x16x32_bf16 v[110:113], v[166:169], v[236:239], v[110:113]
	v_mfma_f32_16x16x32_bf16 v[106:109], v[144:147], v[244:247], v[106:109]
	v_mfma_f32_16x16x32_bf16 v[102:105], v[166:169], v[244:247], v[102:105]
	s_setprio 0
	s_setprio 1
	v_mfma_f32_16x16x32_bf16 v[98:101], v[170:173], v[198:201], v[98:101]
	v_mfma_f32_16x16x32_bf16 v[94:97], v[190:193], v[198:201], v[94:97]
	v_mfma_f32_16x16x32_bf16 v[90:93], v[170:173], v[224:227], v[90:93]
	v_mfma_f32_16x16x32_bf16 v[86:89], v[190:193], v[224:227], v[86:89]
	v_mfma_f32_16x16x32_bf16 v[82:85], v[170:173], v[232:235], v[82:85]
	v_mfma_f32_16x16x32_bf16 v[78:81], v[190:193], v[232:235], v[78:81]
	v_mfma_f32_16x16x32_bf16 v[74:77], v[170:173], v[240:243], v[74:77]
	v_mfma_f32_16x16x32_bf16 v[70:73], v[190:193], v[240:243], v[70:73]
	v_mfma_f32_16x16x32_bf16 v[98:101], v[182:185], v[218:221], v[98:101]
	v_mfma_f32_16x16x32_bf16 v[94:97], v[194:197], v[218:221], v[94:97]
	v_mfma_f32_16x16x32_bf16 v[90:93], v[182:185], v[228:231], v[90:93]
	v_mfma_f32_16x16x32_bf16 v[86:89], v[194:197], v[228:231], v[86:89]
	v_mfma_f32_16x16x32_bf16 v[82:85], v[182:185], v[236:239], v[82:85]
	v_mfma_f32_16x16x32_bf16 v[78:81], v[194:197], v[236:239], v[78:81]
	v_mfma_f32_16x16x32_bf16 v[74:77], v[182:185], v[244:247], v[74:77]
	v_mfma_f32_16x16x32_bf16 v[70:73], v[194:197], v[244:247], v[70:73]
	s_setprio 0
	s_barrier
	s_mov_b64 s[52:53], 0x80
	s_add_i32 s40, s46, s67
	v_lshl_add_u64 v[148:149], v[148:149], 0, s[52:53]
	s_mov_b32 m0, s40
	ds_read_b128 v[198:201], v180 offset:49152
	ds_read_b128 v[218:221], v180 offset:50176
	ds_read_b128 v[224:227], v180 offset:51200
	ds_read_b128 v[228:231], v180 offset:52224
	ds_read_b128 v[232:235], v180 offset:53248
	ds_read_b128 v[236:239], v180 offset:54272
	ds_read_b128 v[240:243], v180 offset:55296
	ds_read_b128 v[244:247], v180 offset:56320
	global_load_lds_dwordx4 v[148:149], off
	s_add_i32 m0, s40, 0x2000
	s_add_u32 s40, s54, 0x40080
	v_lshl_add_u64 v[148:149], v[202:203], 0, s[52:53]
	s_addc_u32 s41, s55, 0
	s_add_i32 s46, s47, s67
	global_load_lds_dwordx4 v[148:149], off
	v_lshl_add_u64 v[148:149], s[40:41], 0, v[150:151]
	s_mov_b32 m0, s46
	s_nop 0
	global_load_lds_dwordx4 v[148:149], off
	s_add_i32 m0, s46, 0x2000
	v_lshl_add_u64 v[148:149], s[40:41], 0, v[152:153]
	s_add_u32 s40, s44, s56
	global_load_lds_dwordx4 v[148:149], off
	s_addc_u32 s41, s33, 0
	s_mov_b32 m0, s76
	s_nop 0
	global_load_lds_dwordx4 v0, s[40:41]
	s_mov_b32 m0, s77
	s_nop 0
	global_load_lds_dwordx4 v139, s[40:41]
	s_waitcnt vmcnt(8)
	v_lshl_add_u32 v181, v250, 11, v176
	v_lshl_add_u32 v186, v249, 11, v177
	v_lshl_add_u32 v188, v248, 11, v176
	v_lshl_add_u32 v187, v223, 11, v177
	s_waitcnt lgkmcnt(0)
	s_barrier
	s_setprio 1
	s_waitcnt lgkmcnt(0)
	v_mfma_f32_16x16x32_bf16 v[66:69], v[140:143], v[198:201], v[66:69]
	v_mfma_f32_16x16x32_bf16 v[62:65], v[162:165], v[198:201], v[62:65]
	v_mfma_f32_16x16x32_bf16 v[58:61], v[140:143], v[224:227], v[58:61]
	v_mfma_f32_16x16x32_bf16 v[54:57], v[162:165], v[224:227], v[54:57]
	v_mfma_f32_16x16x32_bf16 v[50:53], v[140:143], v[232:235], v[50:53]
	v_mfma_f32_16x16x32_bf16 v[46:49], v[162:165], v[232:235], v[46:49]
	v_mfma_f32_16x16x32_bf16 v[42:45], v[140:143], v[240:243], v[42:45]
	v_mfma_f32_16x16x32_bf16 v[38:41], v[162:165], v[240:243], v[38:41]
	v_mfma_f32_16x16x32_bf16 v[66:69], v[144:147], v[218:221], v[66:69]
	v_mfma_f32_16x16x32_bf16 v[62:65], v[166:169], v[218:221], v[62:65]
	v_mfma_f32_16x16x32_bf16 v[58:61], v[144:147], v[228:231], v[58:61]
	v_mfma_f32_16x16x32_bf16 v[54:57], v[166:169], v[228:231], v[54:57]
	v_mfma_f32_16x16x32_bf16 v[50:53], v[144:147], v[236:239], v[50:53]
	v_mfma_f32_16x16x32_bf16 v[46:49], v[166:169], v[236:239], v[46:49]
	v_mfma_f32_16x16x32_bf16 v[42:45], v[144:147], v[244:247], v[42:45]
	v_mfma_f32_16x16x32_bf16 v[38:41], v[166:169], v[244:247], v[38:41]
	s_setprio 0
	s_setprio 1
	v_mfma_f32_16x16x32_bf16 v[30:33], v[170:173], v[198:201], v[30:33]
	v_mfma_f32_16x16x32_bf16 v[26:29], v[190:193], v[198:201], v[26:29]
	v_mfma_f32_16x16x32_bf16 v[22:25], v[170:173], v[224:227], v[22:25]
	v_mfma_f32_16x16x32_bf16 v[18:21], v[190:193], v[224:227], v[18:21]
	v_mfma_f32_16x16x32_bf16 v[14:17], v[170:173], v[232:235], v[14:17]
	v_mfma_f32_16x16x32_bf16 v[10:13], v[190:193], v[232:235], v[10:13]
	v_mfma_f32_16x16x32_bf16 v[6:9], v[170:173], v[240:243], v[6:9]
	v_mfma_f32_16x16x32_bf16 v[2:5], v[190:193], v[240:243], v[2:5]
	v_mfma_f32_16x16x32_bf16 v[30:33], v[182:185], v[218:221], v[30:33]
	v_mfma_f32_16x16x32_bf16 v[26:29], v[194:197], v[218:221], v[26:29]
	v_mfma_f32_16x16x32_bf16 v[22:25], v[182:185], v[228:231], v[22:25]
	v_mfma_f32_16x16x32_bf16 v[18:21], v[194:197], v[228:231], v[18:21]
	v_mfma_f32_16x16x32_bf16 v[14:17], v[182:185], v[236:239], v[14:17]
	v_mfma_f32_16x16x32_bf16 v[10:13], v[194:197], v[236:239], v[10:13]
	v_mfma_f32_16x16x32_bf16 v[6:9], v[182:185], v[244:247], v[6:9]
	v_mfma_f32_16x16x32_bf16 v[2:5], v[194:197], v[244:247], v[2:5]
	s_setprio 0
	s_barrier
	s_add_i32 s13, s13, 2
	s_cmp_gt_u32 s13, 13
	s_cbranch_scc1 .LBB0_2065
	s_mov_b64 s[52:53], s[50:51]
	v_mov_b32_e32 v0, v138
	s_branch .LBB0_2061

.LBB0_2072:
	s_mov_b32 s12, s28
	s_mov_b32 s60, s80
	s_mov_b32 s10, s30
	s_branch .LBB0_2076
